# speedup vs baseline: 1.0279x; 1.0233x over previous
_Z11k_conv_mfmaPKDF16_PKDv8_DF16_PKfS5_S5_S5_S5_PDF16_:
	s_load_dwordx4 s[8:11], s[0:1], 0x0
	s_lshr_b32 s6, s2, 1
	v_readfirstlane_b32 s24, v0
	s_and_b32 s25, s2, 3
	s_and_b32 s3, s6, 2
	s_lshr_b32 s4, s2, 7
	s_lshr_b32 s2, s2, 3
	s_lshr_b32 s23, s24, 6
	s_add_i32 s7, s3, s4
	s_and_b32 s22, s2, 12
	s_mul_i32 s2, s25, 0x65400
	v_and_b32_e32 v1, 63, v0
	s_waitcnt lgkmcnt(0)
	s_lshl_b32 s21, s7, 2
	s_and_b32 s20, s6, 12
	s_add_i32 s12, s20, -1
	v_mul_u32_u24_e32 v16, 0xccd, v1
	v_add_u32_e32 v17, 64, v1
	v_lshrrev_b32_e32 v16, 16, v16
	v_mul_u32_u24_e32 v18, 0xccd, v17
	v_lshlrev_b32_e32 v19, 4, v1
	v_lshrrev_b32_e32 v18, 16, v18
	v_lshlrev_b32_e32 v21, 4, v17
	v_lshl_add_u32 v20, v16, 5, v19
	v_lshl_add_u32 v22, v18, 5, v21
	v_add_u32_e32 v23, s12, v16
	v_add_u32_e32 v17, s12, v18
	v_cmp_gt_u32_e64 s[14:15], 16, v23
	v_cmp_gt_u32_e64 s[16:17], 16, v17
	v_cmp_gt_u32_e64 s[18:19], 56, v1
	v_mov_b64_e32 v[24:25], 0
	v_mov_b64_e32 v[26:27], 0
	v_mov_b64_e32 v[28:29], 0
	v_mov_b64_e32 v[30:31], 0
	v_mov_b64_e32 v[32:33], 0
	v_mov_b64_e32 v[34:35], 0
	v_mov_b64_e32 v[36:37], 0
	v_mov_b64_e32 v[38:39], 0
	v_mov_b64_e32 v[40:41], 0
	v_mov_b64_e32 v[42:43], 0
	v_mov_b64_e32 v[44:45], 0
	v_mov_b64_e32 v[46:47], 0
	v_mov_b64_e32 v[102:103], 0
	v_mov_b64_e32 v[104:105], 0
	v_mov_b64_e32 v[106:107], 0
	v_mov_b64_e32 v[108:109], 0
	v_mov_b64_e32 v[110:111], 0
	v_mov_b64_e32 v[112:113], 0
	v_mov_b64_e32 v[114:115], 0
	v_mov_b64_e32 v[116:117], 0
	s_and_b64 s[16:17], s[16:17], s[18:19]
	s_add_i32 s26, s23, 0
	s_mul_i32 s27, s26, 43
	s_lshr_b32 s27, s27, 8
	s_mul_i32 s28, s27, 6
	s_sub_i32 s28, s26, s28
	s_add_i32 s27, s27, s21
	s_add_i32 s28, s28, s22
	s_add_i32 s27, s27, -1
	s_add_i32 s28, s28, -1
	s_or_b32 s29, s27, s28
	s_cmp_lt_u32 s29, 16
	s_cbranch_scc0 .Lmy_conv_skip0
	s_lshl_b32 s27, s27, 8
	s_lshl_b32 s28, s28, 4
	s_add_i32 s27, s27, s28
	s_add_i32 s27, s27, s12
	s_mulk_i32 s27, 0x140
	s_ashr_i32 s28, s27, 31
	s_add_u32 s34, s8, s27
	s_addc_u32 s35, s9, s28
	s_mov_b64 exec, s[14:15]
	global_load_dwordx4 v[24:27], v19, s[34:35]
	s_mov_b64 exec, s[16:17]
	global_load_dwordx4 v[28:31], v21, s[34:35]
	s_mov_b64 exec, -1
.Lmy_conv_skip0:
	s_add_i32 s26, s23, 8
	s_mul_i32 s27, s26, 43
	s_lshr_b32 s27, s27, 8
	s_mul_i32 s28, s27, 6
	s_sub_i32 s28, s26, s28
	s_add_i32 s27, s27, s21
	s_add_i32 s28, s28, s22
	s_add_i32 s27, s27, -1
	s_add_i32 s28, s28, -1
	s_or_b32 s29, s27, s28
	s_cmp_lt_u32 s29, 16
	s_cbranch_scc0 .Lmy_conv_skip1
	s_lshl_b32 s27, s27, 8
	s_lshl_b32 s28, s28, 4
	s_add_i32 s27, s27, s28
	s_add_i32 s27, s27, s12
	s_mulk_i32 s27, 0x140
	s_ashr_i32 s28, s27, 31
	s_add_u32 s34, s8, s27
	s_addc_u32 s35, s9, s28
	s_mov_b64 exec, s[14:15]
	global_load_dwordx4 v[32:35], v19, s[34:35]
	s_mov_b64 exec, s[16:17]
	global_load_dwordx4 v[36:39], v21, s[34:35]
	s_mov_b64 exec, -1
.Lmy_conv_skip1:
	s_add_i32 s26, s23, 16
	s_mul_i32 s27, s26, 43
	s_lshr_b32 s27, s27, 8
	s_mul_i32 s28, s27, 6
	s_sub_i32 s28, s26, s28
	s_add_i32 s27, s27, s21
	s_add_i32 s28, s28, s22
	s_add_i32 s27, s27, -1
	s_add_i32 s28, s28, -1
	s_or_b32 s29, s27, s28
	s_cmp_lt_u32 s29, 16
	s_cbranch_scc0 .Lmy_conv_skip2
	s_lshl_b32 s27, s27, 8
	s_lshl_b32 s28, s28, 4
	s_add_i32 s27, s27, s28
	s_add_i32 s27, s27, s12
	s_mulk_i32 s27, 0x140
	s_ashr_i32 s28, s27, 31
	s_add_u32 s34, s8, s27
	s_addc_u32 s35, s9, s28
	s_mov_b64 exec, s[14:15]
	global_load_dwordx4 v[40:43], v19, s[34:35]
	s_mov_b64 exec, s[16:17]
	global_load_dwordx4 v[44:47], v21, s[34:35]
	s_mov_b64 exec, -1
.Lmy_conv_skip2:
	s_add_i32 s26, s23, 24
	s_mul_i32 s27, s26, 43
	s_lshr_b32 s27, s27, 8
	s_mul_i32 s28, s27, 6
	s_sub_i32 s28, s26, s28
	s_add_i32 s27, s27, s21
	s_add_i32 s28, s28, s22
	s_add_i32 s27, s27, -1
	s_add_i32 s28, s28, -1
	s_or_b32 s29, s27, s28
	s_cmp_lt_u32 s29, 16
	s_cbranch_scc0 .Lmy_conv_skip3
	s_lshl_b32 s27, s27, 8
	s_lshl_b32 s28, s28, 4
	s_add_i32 s27, s27, s28
	s_add_i32 s27, s27, s12
	s_mulk_i32 s27, 0x140
	s_ashr_i32 s28, s27, 31
	s_add_u32 s34, s8, s27
	s_addc_u32 s35, s9, s28
	s_mov_b64 exec, s[14:15]
	global_load_dwordx4 v[102:105], v19, s[34:35]
	s_mov_b64 exec, s[16:17]
	global_load_dwordx4 v[106:109], v21, s[34:35]
	s_mov_b64 exec, -1
.Lmy_conv_skip3:
	s_cmp_gt_u32 s23, 3
	s_cbranch_scc1 .Lmy_conv_skip4
	s_add_i32 s26, s23, 32
	s_mul_i32 s27, s26, 43
	s_lshr_b32 s27, s27, 8
	s_mul_i32 s28, s27, 6
	s_sub_i32 s28, s26, s28
	s_add_i32 s27, s27, s21
	s_add_i32 s28, s28, s22
	s_add_i32 s27, s27, -1
	s_add_i32 s28, s28, -1
	s_or_b32 s29, s27, s28
	s_cmp_lt_u32 s29, 16
	s_cbranch_scc0 .Lmy_conv_skip4
	s_lshl_b32 s27, s27, 8
	s_lshl_b32 s28, s28, 4
	s_add_i32 s27, s27, s28
	s_add_i32 s27, s27, s12
	s_mulk_i32 s27, 0x140
	s_ashr_i32 s28, s27, 31
	s_add_u32 s34, s8, s27
	s_addc_u32 s35, s9, s28
	s_mov_b64 exec, s[14:15]
	global_load_dwordx4 v[110:113], v19, s[34:35]
	s_mov_b64 exec, s[16:17]
	global_load_dwordx4 v[114:117], v21, s[34:35]
	s_mov_b64 exec, -1
.Lmy_conv_skip4:
	s_add_u32 s4, s10, s2
	v_mov_b32_e32 v10, 0
	s_addc_u32 s5, s11, 0
	v_lshlrev_b32_e32 v2, 4, v1
	v_mov_b32_e32 v3, v10
	v_lshl_add_u64 v[130:131], s[4:5], 0, v[2:3]
	v_and_b32_e32 v2, 8, v0
	v_lshlrev_b32_e32 v2, 4, v2
	s_mul_i32 s2, s23, 0xc0
	s_mov_b32 s3, 0
	v_sub_co_u32_e32 v132, vcc, v130, v2
	s_ashr_i32 s5, s2, 31
	s_mov_b32 s4, s2
	v_subbrev_co_u32_e32 v133, vcc, 0, v131, vcc
	v_lshl_add_u64 v[12:13], s[2:3], 4, v[130:131]
	s_lshl_b64 s[4:5], s[4:5], 4
	v_lshl_add_u64 v[14:15], v[130:131], 0, s[4:5]
	global_load_dwordx4 v[2:5], v[12:13], off
	global_load_dwordx4 v[6:9], v[14:15], off offset:1024
	v_lshl_add_u64 v[12:13], v[132:133], 0, s[4:5]
	s_add_i32 s4, s2, 0x600
	s_mov_b32 s5, s3
	v_lshl_add_u64 v[14:15], s[4:5], 4, v[130:131]
	s_ashr_i32 s5, s4, 31
	s_lshl_b64 s[4:5], s[4:5], 4
	global_load_dwordx4 v[98:101], v[12:13], off offset:2048
	global_load_dwordx4 v[86:89], v[14:15], off
	v_lshl_add_u64 v[12:13], v[130:131], 0, s[4:5]
	v_lshl_add_u64 v[14:15], v[132:133], 0, s[4:5]
	s_add_i32 s4, s2, 0xc00
	s_mov_b32 s5, s3
	global_load_dwordx4 v[90:93], v[12:13], off offset:1024
	global_load_dwordx4 v[94:97], v[14:15], off offset:2048
	v_lshl_add_u64 v[12:13], s[4:5], 4, v[130:131]
	s_ashr_i32 s5, s4, 31
	s_lshl_b64 s[4:5], s[4:5], 4
	v_lshl_add_u64 v[14:15], v[130:131], 0, s[4:5]
	global_load_dwordx4 v[74:77], v[12:13], off
	global_load_dwordx4 v[78:81], v[14:15], off offset:1024
	v_lshl_add_u64 v[12:13], v[132:133], 0, s[4:5]
	s_add_i32 s4, s2, 0x1200
	s_mov_b32 s5, s3
	v_lshl_add_u64 v[14:15], s[4:5], 4, v[130:131]
	s_ashr_i32 s5, s4, 31
	s_lshl_b64 s[4:5], s[4:5], 4
	global_load_dwordx4 v[82:85], v[12:13], off offset:2048
	global_load_dwordx4 v[62:65], v[14:15], off
	v_lshl_add_u64 v[12:13], v[130:131], 0, s[4:5]
	s_addk_i32 s2, 0x1800
	v_lshl_add_u64 v[14:15], v[132:133], 0, s[4:5]
	global_load_dwordx4 v[66:69], v[12:13], off offset:1024
	global_load_dwordx4 v[70:73], v[14:15], off offset:2048
	v_lshl_add_u64 v[12:13], s[2:3], 4, v[130:131]
	s_ashr_i32 s3, s2, 31
	s_lshl_b64 s[2:3], s[2:3], 4
	v_lshl_add_u64 v[14:15], v[130:131], 0, s[2:3]
	global_load_dwordx4 v[50:53], v[12:13], off
	global_load_dwordx4 v[54:57], v[14:15], off offset:1024
	v_lshl_add_u64 v[12:13], v[132:133], 0, s[2:3]
	global_load_dwordx4 v[58:61], v[12:13], off offset:2048
	s_load_dwordx8 s[4:11], s[0:1], 0x10
	s_load_dwordx2 s[12:13], s[0:1], 0x30
	s_mul_i32 s26, s23, 0x840
	v_add_u32_e32 v20, s26, v20
	v_add_u32_e32 v22, s26, v22
	s_waitcnt vmcnt(15)
	ds_write_b128 v20, v[24:27]
	ds_write_b128 v20, v[32:35] offset:16896
	ds_write_b128 v20, v[40:43] offset:33792
	ds_write_b128 v20, v[102:105] offset:50688
	s_mov_b64 exec, s[18:19]
	ds_write_b128 v22, v[28:31]
	ds_write_b128 v22, v[36:39] offset:16896
	ds_write_b128 v22, v[44:47] offset:33792
	ds_write_b128 v22, v[106:109] offset:50688
	s_mov_b64 exec, -1
	s_cmp_gt_u32 s23, 3
	s_cbranch_scc1 .Lmy_conv_nor5
	v_add_u32_e32 v20, 0x10800, v20
	v_add_u32_e32 v22, 0x10800, v22
	ds_write_b128 v20, v[110:113]
	s_mov_b64 exec, s[18:19]
	ds_write_b128 v22, v[114:117]
	s_mov_b64 exec, -1
.Lmy_conv_nor5:
	v_and_b32_e32 v135, 15, v0
	s_mul_i32 s25, s25, 40
	v_add_lshl_u32 v10, v135, s25, 2
	v_or_b32_e32 v11, 32, v135
	s_waitcnt lgkmcnt(0)
	global_load_dword v14, v10, s[12:13]
	global_load_dword v140, v10, s[4:5]
	global_load_dword v141, v10, s[10:11]
	global_load_dword v134, v10, s[8:9]
	global_load_dword v138, v10, s[6:7] offset:64
	global_load_dword v139, v10, s[4:5] offset:64
	global_load_dword v15, v10, s[12:13] offset:64
	v_cmp_gt_u32_e32 vcc, 40, v11
	s_min_u32 s2, s23, 0x5e
	s_mulk_i32 s2, 0xc00
	v_cndmask_b32_e32 v11, 0, v11, vcc
	v_add_lshl_u32 v11, v11, s25, 2
	global_load_dword v142, v11, s[4:5]
	global_load_dword v143, v11, s[10:11]
	global_load_dword v136, v11, s[8:9]
	global_load_dword v16, v11, s[12:13]
	global_load_dword v146, v10, s[6:7]
	global_load_dword v144, v11, s[6:7]
	s_mov_b32 s19, 0
	s_add_i32 s18, s2, 0x1e000
	global_load_dword v145, v10, s[10:11] offset:64
	global_load_dword v137, v10, s[8:9] offset:64
	v_lshl_add_u64 v[10:11], v[130:131], 0, s[18:19]
	v_lshl_add_u64 v[12:13], v[132:133], 0, s[18:19]
	s_barrier
	global_load_dwordx4 v[102:105], v[10:11], off
	global_load_dwordx4 v[106:109], v[10:11], off offset:1024
	global_load_dwordx4 v[110:113], v[12:13], off offset:2048
	v_and_b32_e32 v11, 3, v0
	v_bfe_u32 v12, v0, 2, 2
	s_mov_b32 s4, 0xf800000
	v_mad_u32_u24 v11, v11, 6, v12
	v_and_b32_e32 v10, 48, v0
	s_movk_i32 s18, 0x160
	v_mad_u32_u24 v150, v11, s18, v10
	s_waitcnt vmcnt(17)
	v_add_f32_e32 v12, 0x3727c5ac, v14
	v_mul_f32_e32 v14, 0x4f800000, v12
	v_cmp_gt_f32_e32 vcc, s4, v12
	s_waitcnt vmcnt(11)
	v_add_f32_e32 v13, 0x3727c5ac, v15
	v_mul_f32_e32 v15, 0x4f800000, v13
	v_cndmask_b32_e32 v147, v12, v14, vcc
	v_cmp_gt_f32_e64 s[2:3], s4, v13
	s_waitcnt vmcnt(7)
	v_add_f32_e32 v12, 0x3727c5ac, v16
	v_cmp_gt_f32_e64 s[4:5], s4, v12
	v_cndmask_b32_e64 v148, v13, v15, s[2:3]
	v_mul_f32_e32 v13, 0x4f800000, v12
	v_sqrt_f32_e32 v154, v147
	v_cndmask_b32_e64 v149, v12, v13, s[4:5]
	v_sqrt_f32_e32 v155, v148
	v_sqrt_f32_e32 v156, v149
	v_add_u32_e32 v157, -1, v154
	v_add_u32_e32 v151, 1, v154
	v_add_u32_e32 v158, -1, v155
	v_add_u32_e32 v152, 1, v155
	v_fma_f32 v12, -v157, v154, v147
	v_fma_f32 v13, -v151, v154, v147
	v_add_u32_e32 v159, -1, v156
	v_add_u32_e32 v153, 1, v156
	v_fma_f32 v14, -v158, v155, v148
	v_fma_f32 v15, -v152, v155, v148
	v_cmp_ge_f32_e64 s[12:13], 0, v12
	v_cmp_lt_f32_e64 s[6:7], 0, v13
	v_fma_f32 v12, -v159, v156, v149
	v_fma_f32 v13, -v153, v156, v149
	v_cmp_ge_f32_e64 s[14:15], 0, v14
	v_cmp_lt_f32_e64 s[8:9], 0, v15
	v_cmp_ge_f32_e64 s[16:17], 0, v12
	v_cmp_lt_f32_e64 s[10:11], 0, v13
	s_cmpk_gt_u32 s24, 0x21bf
	s_cbranch_scc1 .LBB0_24
	s_mul_i32 s27, s23, 0x6d
	s_lshr_b32 s28, s27, 8
	s_sub_i32 s28, s23, s28
	s_bfe_u32 s28, s28, 0x70001
	s_bfe_u32 s27, s27, 0x80008
	s_add_i32 s28, s28, s27
	s_bfe_u32 s27, s28, 0x30005
	s_mul_i32 s28, s23, 0x89
	s_bfe_u32 s28, s28, 0x5000b
	s_mul_i32 s29, s28, 0x56
	s_mul_i32 s18, s23, 0xcd
	s_bfe_u32 s29, s29, 0x80008
	s_bfe_u32 s18, s18, 0x6000a
	s_mul_i32 s29, s29, 3
	s_sub_i32 s28, s28, s29
	s_mul_i32 s29, s18, 0x56
	s_bfe_u32 s29, s29, 0x80008
	s_mul_i32 s29, s29, 3
	s_mul_i32 s26, s18, -5
	s_sub_i32 s18, s18, s29
	s_mul_i32 s27, s27, 36
	s_mul_i32 s28, s28, 6
	s_or_b32 s18, s18, s27
	s_add_i32 s18, s18, s28
	s_add_i32 s26, s26, s23
	s_and_b32 s18, s18, 0xff
	s_mulk_i32 s18, 0x160
	s_lshl_b32 s26, s26, 6
	s_add_i32 s26, s26, s18
	v_add_u32_e32 v14, s26, v150
	ds_read_b128 v[10:13], v14
	ds_read_b128 v[114:117], v14 offset:38016
	s_waitcnt lgkmcnt(1)
	v_mfma_f32_16x16x32_f16 v[46:49], v[10:13], v[2:5], 0
	v_mfma_f32_16x16x32_f16 v[42:45], v[10:13], v[6:9], 0
	v_mfma_f32_16x16x32_f16 v[34:37], v[10:13], v[98:101], 0
	ds_read_b128 v[10:13], v14 offset:12672
	ds_read_b128 v[14:17], v14 offset:25344
	s_waitcnt lgkmcnt(1)
	v_mfma_f32_16x16x32_f16 v[38:41], v[10:13], v[2:5], 0
	v_mfma_f32_16x16x32_f16 v[30:33], v[10:13], v[6:9], 0
	v_mfma_f32_16x16x32_f16 v[26:29], v[10:13], v[98:101], 0
	s_waitcnt lgkmcnt(0)
	v_mfma_f32_16x16x32_f16 v[22:25], v[14:17], v[2:5], 0
	v_mfma_f32_16x16x32_f16 v[18:21], v[14:17], v[6:9], 0
	v_mfma_f32_16x16x32_f16 v[14:17], v[14:17], v[98:101], 0
	v_mfma_f32_16x16x32_f16 v[10:13], v[114:117], v[2:5], 0
	v_mfma_f32_16x16x32_f16 v[6:9], v[114:117], v[6:9], 0
	v_mfma_f32_16x16x32_f16 v[2:5], v[114:117], v[98:101], 0
	s_branch .LBB0_25

.LBB1_2:
	s_or_b64 exec, exec, s[10:11]
	s_lshl_b32 s7, s2, 1
	s_bfe_u32 s2, s2, 0x10003
	v_readfirstlane_b32 s6, v0
	s_and_b32 s7, s7, 14
	s_or_b32 s7, s7, s2
	s_lshr_b32 s10, s6, 2
	s_lshl_b32 s2, s7, 8
	s_and_b32 s10, s10, 0x3ffffff0
	v_and_b32_e32 v1, 15, v0
	s_add_i32 s10, s10, s2
	v_or_b32_e32 v4, s10, v1
	s_movk_i32 s2, 0x140
	v_mov_b64_e32 v[2:3], s[4:5]
	v_mad_u64_u32 v[2:3], s[4:5], v4, s2, v[2:3]
	v_and_b32_e32 v30, 48, v0
	v_lshl_add_u64 v[32:33], v[2:3], 0, v[30:31]
	s_mul_i32 s3, s3, 10
	v_bfe_u32 v30, v0, 5, 1
	v_or_b32_e32 v30, s3, v30
	v_lshl_add_u64 v[42:43], v[30:31], 2, s[8:9]
	global_load_dwordx4 v[18:21], v[32:33], off
	global_load_dwordx4 v[14:17], v[32:33], off offset:64
	global_load_dwordx4 v[10:13], v[32:33], off offset:128
	global_load_dwordx4 v[6:9], v[32:33], off offset:192
	global_load_dwordx4 v[2:5], v[32:33], off offset:256
	global_load_dword v40, v[42:43], off
	global_load_dword v38, v[42:43], off offset:8
	global_load_dword v36, v[42:43], off offset:16
	global_load_dword v34, v[42:43], off offset:24
	s_nop 0
	global_load_dword v32, v[42:43], off offset:32
	s_load_dwordx2 s[0:1], s[0:1], 0x18
	v_and_b32_e32 v35, 63, v0
	v_bfe_u32 v33, v0, 4, 2
	v_lshlrev_b32_e32 v0, 4, v0
	s_waitcnt vmcnt(10)
	ds_write_b128 v0, v[26:29]
	s_and_saveexec_b64 s[2:3], vcc
	ds_write_b128 v0, v[22:25] offset:16384
	s_or_b64 exec, exec, s[2:3]
	v_lshlrev_b32_e32 v35, 4, v35
	s_waitcnt lgkmcnt(0)
	s_barrier
	ds_read_b128 v[22:25], v35
	ds_read_b128 v[26:29], v35 offset:1024
	ds_read_b128 v[46:49], v35 offset:2048
	s_waitcnt vmcnt(9) lgkmcnt(2)
	v_mfma_f32_16x16x32_f16 v[22:25], v[22:25], v[18:21], 0
	ds_read_b128 v[42:45], v35 offset:5120
	ds_read_b128 v[50:53], v35 offset:8192
	v_lshlrev_b32_e32 v0, 12, v33
	s_waitcnt vmcnt(8) lgkmcnt(3)
	v_mfma_f32_16x16x32_f16 v[22:25], v[26:29], v[14:17], v[22:25]
	ds_read_b128 v[26:29], v35 offset:3072
	v_mov_b32_e32 v55, 0
	v_and_b32_e32 v0, 0x1000, v0
	s_waitcnt vmcnt(7) lgkmcnt(3)
	v_mfma_f32_16x16x32_f16 v[22:25], v[46:49], v[10:13], v[22:25]
	ds_read_b128 v[46:49], v35 offset:4096
	v_lshl_or_b32 v58, s7, 13, v0
	v_mov_b32_e32 v59, v55
	s_waitcnt vmcnt(6) lgkmcnt(1)
	v_mfma_f32_16x16x32_f16 v[22:25], v[26:29], v[6:9], v[22:25]
	ds_read_b128 v[26:29], v35 offset:6144
	v_lshlrev_b32_e32 v0, 3, v1
	v_and_b32_e32 v64, 1, v1
	s_movk_i32 s18, 0x78
	v_mad_u32_u24 v0, v64, s18, v0
	s_mov_b32 s14, 0x55555555
	s_mov_b32 s15, 0x55555555
	s_not_b64 s[16:17], s[14:15]
	v_mov_b32_e32 v1, v55
	s_waitcnt vmcnt(5) lgkmcnt(1)
	v_mfma_f32_16x16x32_f16 v[22:25], v[46:49], v[2:5], v[22:25]
	ds_read_b128 v[46:49], v35 offset:7168
	v_add_u32_e32 v54, 2, v30
	v_add_u32_e32 v56, 4, v30
	v_mfma_f32_16x16x32_f16 v[42:45], v[42:45], v[18:21], 0
	v_mov_b32_e32 v57, v55
	s_waitcnt vmcnt(4)
	s_nop 1
	v_pk_add_f32 v[60:61], v[22:23], v[40:41] op_sel_hi:[1,0]
	v_pk_add_f32 v[62:63], v[24:25], v[40:41] op_sel_hi:[1,0]
	s_waitcnt lgkmcnt(1)
	v_mfma_f32_16x16x32_f16 v[26:29], v[26:29], v[14:17], v[42:45]
	s_waitcnt lgkmcnt(0)
	v_mfma_f32_16x16x32_f16 v[26:29], v[46:49], v[10:13], v[26:29]
	s_nop 0
	ds_read_b128 v[42:45], v35 offset:9216
	ds_read_b128 v[46:49], v35 offset:10240
	v_mfma_f32_16x16x32_f16 v[26:29], v[50:53], v[6:9], v[26:29]
	ds_read_b128 v[50:53], v35 offset:11264
	s_waitcnt lgkmcnt(2)
	v_mfma_f32_16x16x32_f16 v[26:29], v[42:45], v[2:5], v[26:29]
	ds_read_b128 v[40:43], v35 offset:12288
	s_waitcnt lgkmcnt(2)
	v_mfma_f32_16x16x32_f16 v[22:25], v[46:49], v[18:21], 0
	ds_read_b128 v[44:47], v35 offset:13312
	v_lshl_add_u64 v[48:49], s[0:1], 0, v[58:59]
	s_and_b32 s0, s6, 0xffffffc0
	s_waitcnt lgkmcnt(2)
	v_mfma_f32_16x16x32_f16 v[22:25], v[50:53], v[14:17], v[22:25]
	s_ashr_i32 s1, s0, 31
	v_lshl_add_u64 v[48:49], s[0:1], 2, v[48:49]
	v_lshl_add_u64 v[0:1], v[48:49], 0, v[0:1]
	s_waitcnt lgkmcnt(1)
	v_mfma_f32_16x16x32_f16 v[22:25], v[40:43], v[10:13], v[22:25]
	ds_read_b128 v[40:43], v35 offset:14336
	v_lshlrev_b64 v[48:49], 17, v[30:31]
	v_lshl_add_u64 v[48:49], v[0:1], 0, v[48:49]
	s_waitcnt lgkmcnt(1)
	v_mfma_f32_16x16x32_f16 v[22:25], v[44:47], v[6:9], v[22:25]
	ds_read_b128 v[44:47], v35 offset:15360
	s_mov_b64 vcc, s[14:15]
	v_cndmask_b32_dpp v64, v62, v60, vcc quad_perm:[1,0,3,2] row_mask:0xf bank_mask:0xf
	v_cndmask_b32_dpp v65, v63, v61, vcc quad_perm:[1,0,3,2] row_mask:0xf bank_mask:0xf
	s_mov_b64 vcc, s[16:17]
	v_cndmask_b32_dpp v66, v60, v62, vcc quad_perm:[1,0,3,2] row_mask:0xf bank_mask:0xf
	v_cndmask_b32_dpp v67, v61, v63, vcc quad_perm:[1,0,3,2] row_mask:0xf bank_mask:0xf
	global_store_dwordx4 v[48:49], v[64:67], off sc1
	ds_read_b128 v[48:51], v35 offset:16384
	s_waitcnt vmcnt(4)
	v_pk_add_f32 v[52:53], v[26:27], v[38:39] op_sel_hi:[1,0]
	v_pk_add_f32 v[58:59], v[28:29], v[38:39] op_sel_hi:[1,0]
	ds_read_b128 v[26:29], v35 offset:17408
	s_waitcnt lgkmcnt(3)
	v_mfma_f32_16x16x32_f16 v[22:25], v[40:43], v[2:5], v[22:25]
	v_add_u32_e32 v60, 6, v30
	v_mov_b32_e32 v61, v55
	v_add_u32_e32 v30, 8, v30
	s_waitcnt lgkmcnt(2)
	v_mfma_f32_16x16x32_f16 v[38:41], v[44:47], v[18:21], 0
	ds_read_b128 v[42:45], v35 offset:18432
	v_lshlrev_b64 v[46:47], 17, v[54:55]
	v_lshl_add_u64 v[46:47], v[0:1], 0, v[46:47]
	s_waitcnt lgkmcnt(2)
	v_mfma_f32_16x16x32_f16 v[38:41], v[48:51], v[14:17], v[38:41]
	v_mov_b32_e32 v31, v55
	s_waitcnt lgkmcnt(1)
	v_mfma_f32_16x16x32_f16 v[26:29], v[26:29], v[10:13], v[38:41]
	s_nop 4
	ds_read_b128 v[38:41], v35 offset:19456
	s_mov_b64 vcc, s[14:15]
	v_cndmask_b32_dpp v68, v58, v52, vcc quad_perm:[1,0,3,2] row_mask:0xf bank_mask:0xf
	v_cndmask_b32_dpp v69, v59, v53, vcc quad_perm:[1,0,3,2] row_mask:0xf bank_mask:0xf
	s_mov_b64 vcc, s[16:17]
	v_cndmask_b32_dpp v70, v52, v58, vcc quad_perm:[1,0,3,2] row_mask:0xf bank_mask:0xf
	v_cndmask_b32_dpp v71, v53, v59, vcc quad_perm:[1,0,3,2] row_mask:0xf bank_mask:0xf
	global_store_dwordx4 v[46:47], v[68:71], off sc1
	ds_read_b128 v[46:49], v35 offset:20480
	s_waitcnt lgkmcnt(2)
	v_mfma_f32_16x16x32_f16 v[26:29], v[42:45], v[6:9], v[26:29]
	v_lshlrev_b64 v[42:43], 17, v[56:57]
	v_lshl_add_u64 v[50:51], v[0:1], 0, v[42:43]
	ds_read_b128 v[42:45], v35 offset:21504
	s_waitcnt lgkmcnt(2)
	v_mfma_f32_16x16x32_f16 v[26:29], v[38:41], v[2:5], v[26:29]
	s_waitcnt vmcnt(4)
	v_pk_add_f32 v[38:39], v[22:23], v[36:37] op_sel_hi:[1,0]
	v_pk_add_f32 v[36:37], v[24:25], v[36:37] op_sel_hi:[1,0]
	ds_read_b128 v[22:25], v35 offset:22528
	s_waitcnt lgkmcnt(2)
	v_mfma_f32_16x16x32_f16 v[18:21], v[46:49], v[18:21], 0
	s_mov_b64 vcc, s[14:15]
	v_cndmask_b32_dpp v72, v36, v38, vcc quad_perm:[1,0,3,2] row_mask:0xf bank_mask:0xf
	v_cndmask_b32_dpp v73, v37, v39, vcc quad_perm:[1,0,3,2] row_mask:0xf bank_mask:0xf
	s_mov_b64 vcc, s[16:17]
	v_cndmask_b32_dpp v74, v38, v36, vcc quad_perm:[1,0,3,2] row_mask:0xf bank_mask:0xf
	v_cndmask_b32_dpp v75, v39, v37, vcc quad_perm:[1,0,3,2] row_mask:0xf bank_mask:0xf
	global_store_dwordx4 v[50:51], v[72:75], off sc1
	ds_read_b128 v[36:39], v35 offset:23552
	s_waitcnt lgkmcnt(2)
	v_mfma_f32_16x16x32_f16 v[14:17], v[42:45], v[14:17], v[18:21]
	s_nop 2
	v_lshlrev_b64 v[18:19], 17, v[60:61]
	v_lshl_add_u64 v[40:41], v[0:1], 0, v[18:19]
	ds_read_b128 v[18:21], v35 offset:24576
	s_waitcnt lgkmcnt(2)
	v_mfma_f32_16x16x32_f16 v[10:13], v[22:25], v[10:13], v[14:17]
	s_waitcnt lgkmcnt(1)
	v_mfma_f32_16x16x32_f16 v[6:9], v[36:39], v[6:9], v[10:13]
	s_waitcnt vmcnt(4)
	v_pk_add_f32 v[14:15], v[26:27], v[34:35] op_sel_hi:[1,0]
	v_pk_add_f32 v[16:17], v[28:29], v[34:35] op_sel_hi:[1,0]
	s_nop 1
	v_lshlrev_b64 v[10:11], 17, v[30:31]
	v_lshl_add_u64 v[10:11], v[0:1], 0, v[10:11]
	s_waitcnt lgkmcnt(0)
	v_mfma_f32_16x16x32_f16 v[0:3], v[18:21], v[2:5], v[6:9]
	s_mov_b64 vcc, s[14:15]
	v_cndmask_b32_dpp v76, v16, v14, vcc quad_perm:[1,0,3,2] row_mask:0xf bank_mask:0xf
	v_cndmask_b32_dpp v77, v17, v15, vcc quad_perm:[1,0,3,2] row_mask:0xf bank_mask:0xf
	s_mov_b64 vcc, s[16:17]
	v_cndmask_b32_dpp v78, v14, v16, vcc quad_perm:[1,0,3,2] row_mask:0xf bank_mask:0xf
	v_cndmask_b32_dpp v79, v15, v17, vcc quad_perm:[1,0,3,2] row_mask:0xf bank_mask:0xf
	global_store_dwordx4 v[40:41], v[76:79], off sc1
	s_waitcnt vmcnt(4)
	s_nop 5
	v_pk_add_f32 v[0:1], v[0:1], v[32:33] op_sel_hi:[1,0]
	v_pk_add_f32 v[2:3], v[2:3], v[32:33] op_sel_hi:[1,0]
	s_nop 1
	s_mov_b64 vcc, s[14:15]
	v_cndmask_b32_dpp v80, v2, v0, vcc quad_perm:[1,0,3,2] row_mask:0xf bank_mask:0xf
	v_cndmask_b32_dpp v81, v3, v1, vcc quad_perm:[1,0,3,2] row_mask:0xf bank_mask:0xf
	s_mov_b64 vcc, s[16:17]
	v_cndmask_b32_dpp v82, v0, v2, vcc quad_perm:[1,0,3,2] row_mask:0xf bank_mask:0xf
	v_cndmask_b32_dpp v83, v1, v3, vcc quad_perm:[1,0,3,2] row_mask:0xf bank_mask:0xf
	global_store_dwordx4 v[10:11], v[80:83], off sc1
	s_endpgm

	.amdhsa_kernel _Z12k_recon_mfmaPKDF16_PKDv8_DF16_PKfPf
		.amdhsa_group_segment_fixed_size 25600
		.amdhsa_private_segment_fixed_size 0
		.amdhsa_kernarg_size 32
		.amdhsa_user_sgpr_count 2
		.amdhsa_user_sgpr_dispatch_ptr 0
		.amdhsa_user_sgpr_queue_ptr 0
		.amdhsa_user_sgpr_kernarg_segment_ptr 1
		.amdhsa_user_sgpr_dispatch_id 0
		.amdhsa_user_sgpr_kernarg_preload_length 0
		.amdhsa_user_sgpr_kernarg_preload_offset 0
		.amdhsa_user_sgpr_private_segment_size 0
		.amdhsa_uses_dynamic_stack 0
		.amdhsa_enable_private_segment 0
		.amdhsa_system_sgpr_workgroup_id_x 1
		.amdhsa_system_sgpr_workgroup_id_y 0
		.amdhsa_system_sgpr_workgroup_id_z 0
		.amdhsa_system_sgpr_workgroup_info 0
		.amdhsa_system_vgpr_workitem_id 0
		.amdhsa_next_free_vgpr 84
		.amdhsa_next_free_sgpr 19
		.amdhsa_accum_offset 84
		.amdhsa_reserve_vcc 1
		.amdhsa_float_round_mode_32 0
		.amdhsa_float_round_mode_16_64 0
		.amdhsa_float_denorm_mode_32 3
		.amdhsa_float_denorm_mode_16_64 3
		.amdhsa_dx10_clamp 1
		.amdhsa_ieee_mode 1
		.amdhsa_fp16_overflow 0
		.amdhsa_tg_split 0
		.amdhsa_exception_fp_ieee_invalid_op 0
		.amdhsa_exception_fp_denorm_src 0
		.amdhsa_exception_fp_ieee_div_zero 0
		.amdhsa_exception_fp_ieee_overflow 0
		.amdhsa_exception_fp_ieee_underflow 0
		.amdhsa_exception_fp_ieee_inexact 0
		.amdhsa_exception_int_div_zero 0
	.end_amdhsa_kernel

_Z8k_resid2PKDF16_PKfS0_S2_S2_PDF16_:
	s_load_dwordx2 s[6:7], s[0:1], 0x8
	s_load_dwordx8 s[20:27], s[0:1], 0x0
	s_load_dwordx4 s[28:31], s[0:1], 0x20
	v_mov_b32_e32 v102, 0
	v_mov_b32_e32 v103, 0
	v_mov_b32_e32 v108, 0
	v_mov_b32_e32 v104, 0
	v_mov_b32_e32 v105, 0
	v_mov_b32_e32 v106, 0
	v_mov_b32_e32 v107, 0
	s_lshr_b32 s3, s2, 6
	s_and_b32 s15, s2, 1
	s_mul_i32 s4, s3, 0x500
	s_mul_i32 s8, s15, 0x280
	s_movk_i32 s5, 0x280
	s_add_i32 s4, s4, s8
	v_readfirstlane_b32 s14, v0
	v_cmp_gt_u32_e64 s[8:9], s5, v0
	v_mov_b32_e32 v1, 0
	v_add_u32_e32 v2, s4, v0
	v_mov_b32_e32 v80, 0
	s_waitcnt lgkmcnt(0)
	s_and_saveexec_b64 s[4:5], s[8:9]
	s_cbranch_execz .LBB4_2
	v_mov_b32_e32 v3, 0
	s_waitcnt lgkmcnt(0)
	v_lshl_add_u64 v[4:5], v[2:3], 2, s[6:7]
	global_load_dword v102, v[4:5], off
.LBB4_2:
	s_or_b64 exec, exec, s[4:5]
	s_movk_i32 s4, 0x180
	v_cmp_gt_u32_e32 vcc, s4, v0
	s_and_saveexec_b64 s[4:5], vcc
	s_cbranch_execz .LBB4_4
	v_mov_b32_e32 v3, 0
	s_waitcnt lgkmcnt(0)
	v_lshl_add_u64 v[4:5], v[2:3], 2, s[6:7]
	global_load_dword v103, v[4:5], off offset:1024
.LBB4_4:
	s_or_b64 exec, exec, s[4:5]
	s_mov_b64 s[10:11], s[24:25]
	s_movk_i32 s4, 0x80
	v_cmp_gt_u32_e64 s[4:5], s4, v0
	v_mov_b32_e32 v77, 0
	v_mov_b32_e32 v81, 0
	s_and_saveexec_b64 s[12:13], s[4:5]
	s_cbranch_execz .LBB4_6
	v_mov_b32_e32 v3, 0
	s_waitcnt lgkmcnt(0)
	v_lshl_add_u64 v[2:3], v[2:3], 2, s[6:7]
	global_load_dword v108, v[2:3], off offset:2048
.LBB4_6:
	s_or_b64 exec, exec, s[12:13]
	s_bfe_u32 s17, s2, 0x50001
	v_bfe_u32 v2, v0, 2, 2
	s_lshl_b32 s18, s3, 10
	v_lshl_or_b32 v2, s17, 5, v2
	s_lshr_b32 s16, s14, 6
	v_or_b32_e32 v2, s18, v2
	v_and_b32_e32 v10, 3, v0
	v_lshl_add_u32 v11, s16, 3, v2
	v_mul_u32_u24_e32 v2, 40, v10
	v_lshlrev_b32_e32 v76, 1, v2
	v_bfe_u32 v82, v0, 4, 2
	s_waitcnt lgkmcnt(0)
	v_lshl_add_u64 v[2:3], s[10:11], 0, v[76:77]
	s_movk_i32 s19, 0x140
	v_mad_u64_u32 v[4:5], s[2:3], v11, s19, v[2:3]
	v_lshlrev_b32_e32 v76, 4, v82
	v_lshl_add_u64 v[6:7], v[4:5], 0, v[76:77]
	global_load_dwordx4 v[6:9], v[6:7], off
	s_mov_b64 s[2:3], s[20:21]
	s_mov_b64 s[10:11], s[28:29]
	v_lshlrev_b32_e32 v12, 3, v82
	v_cmp_eq_u32_e64 s[6:7], 0, v82
	v_mov_b32_e32 v90, 0
	v_mov_b32_e32 v91, 0
	v_mov_b32_e32 v92, 0
	v_mov_b32_e32 v93, 0
	s_and_saveexec_b64 s[12:13], s[6:7]
	s_cbranch_execz .LBB4_8
	global_load_dwordx4 v[90:93], v[4:5], off offset:64
.LBB4_8:
	s_or_b64 exec, exec, s[12:13]
	v_or_b32_e32 v4, 4, v11
	v_mad_u64_u32 v[2:3], s[12:13], v4, s19, v[2:3]
	v_lshlrev_b32_e32 v72, 1, v12
	v_mov_b32_e32 v73, 0
	v_lshl_add_u64 v[4:5], v[2:3], 0, v[72:73]
	global_load_dwordx4 v[38:41], v[4:5], off
	v_and_b32_e32 v25, 0xffff, v77
	v_mov_b32_e32 v23, v77
	v_mov_b32_e32 v24, v77
	s_and_saveexec_b64 s[12:13], s[6:7]
	s_cbranch_execz .LBB4_10
	global_load_dwordx4 v[104:107], v[2:3], off offset:64
.LBB4_10:
	s_or_b64 exec, exec, s[12:13]
	v_lshrrev_b32_e32 v84, 4, v0
	s_lshl_b32 s12, s15, 4
	v_or_b32_e32 v2, s12, v84
	v_lshl_add_u32 v2, v2, 5, s18
	v_or_b32_e32 v2, s17, v2
	s_movk_i32 s6, 0xa0
	v_lshlrev_b32_e32 v4, 3, v0
	v_mad_u64_u32 v[78:79], s[6:7], v2, s6, 0
	v_and_b32_e32 v4, 0x78, v4
	s_waitcnt lgkmcnt(0)
	v_lshl_add_u64 v[2:3], v[78:79], 1, s[2:3]
	v_lshlrev_b32_e32 v70, 1, v4
	v_mov_b32_e32 v71, v73
	v_lshl_add_u64 v[2:3], v[2:3], 0, v[70:71]
	v_lshlrev_b32_e32 v85, 2, v4
	global_load_dwordx4 v[46:49], v[2:3], off
	global_load_dwordx4 v[42:45], v85, s[10:11] offset:16
	global_load_dwordx4 v[50:53], v85, s[10:11]
	v_lshrrev_b32_e32 v2, 2, v0
	v_and_or_b32 v2, v2, 15, s12
	v_lshl_or_b32 v2, v2, 5, s18
	s_cmp_lt_u32 s14, 64
	v_or_b32_e32 v76, s17, v2
	s_cselect_b64 s[6:7], -1, 0
	s_cmp_gt_u32 s14, 63
	v_lshlrev_b32_e32 v74, 4, v10
	s_cbranch_scc1 .LBB4_12
	s_mov_b64 s[12:13], s[26:27]
	v_lshl_or_b32 v11, v76, 2, v10
	s_movk_i32 s14, 0x140
	v_mov_b64_e32 v[2:3], s[2:3]
	v_mad_u64_u32 v[2:3], s[2:3], v76, s14, v[2:3]
	s_waitcnt lgkmcnt(0)
	v_mad_u64_u32 v[62:63], s[2:3], v11, 48, s[12:13]
	s_mov_b64 s[2:3], 0xc0000
	s_nop 0
	v_lshl_add_u64 v[14:15], v[62:63], 0, s[2:3]
	s_mov_b32 s2, 0xc0000
	v_add_co_u32_e64 v26, s[2:3], s2, v62
	v_mov_b32_e32 v75, 0
	s_nop 0
	v_addc_co_u32_e64 v27, s[2:3], 0, v63, s[2:3]
	s_mov_b64 s[2:3], 0x180000
	s_nop 0
	v_lshl_add_u64 v[28:29], v[62:63], 0, s[2:3]
	s_mov_b32 s2, 0x180000
	v_add_co_u32_e64 v30, s[2:3], s2, v62
	v_lshl_add_u64 v[2:3], v[2:3], 0, v[74:75]
	s_nop 0
	v_addc_co_u32_e64 v31, s[2:3], 0, v63, s[2:3]
	s_mov_b64 s[2:3], 0x240000
	s_nop 0
	v_lshl_add_u64 v[88:89], v[62:63], 0, s[2:3]
	s_mov_b32 s2, 0x240000
	v_add_co_u32_e64 v94, s[2:3], s2, v62
	global_load_dwordx4 v[2:5], v[2:3], off offset:256
	v_lshlrev_b32_e32 v22, 5, v10
	global_load_dwordx4 v[10:13], v[62:63], off
	global_load_dwordx4 v[34:37], v[62:63], off offset:16
	global_load_dword v73, v[62:63], off offset:32
	global_load_dword v75, v[14:15], off offset:32
	global_load_dwordx4 v[54:57], v[14:15], off offset:16
	s_nop 0
	global_load_dwordx4 v[14:17], v[30:31], off
	global_load_dword v83, v[28:29], off offset:32
	global_load_dwordx4 v[58:61], v[26:27], off
	global_load_dwordx4 v[18:21], v[28:29], off offset:16
	v_addc_co_u32_e64 v95, s[2:3], 0, v63, s[2:3]
	global_load_dwordx4 v[26:29], v22, s[10:11] offset:512
	global_load_dwordx4 v[30:33], v22, s[10:11] offset:528
	global_load_dwordx4 v[62:65], v[94:95], off
	global_load_dword v86, v[88:89], off offset:32
	global_load_dwordx4 v[66:69], v[88:89], off offset:16
	s_waitcnt vmcnt(22)
	v_cvt_f16_f32_e32 v80, v102
	v_cvt_f16_f32_e32 v1, v103
	v_cvt_f16_f32_e32 v81, v108
	v_lshlrev_b32_e32 v87, 1, v0
	s_and_saveexec_b64 s[2:3], s[8:9]
	s_cbranch_execnz .LBB4_13
	s_branch .LBB4_14
.LBB4_12:
	v_mov_b32_e32 v75, 0
	v_mov_b32_e32 v83, 0
	v_mov_b32_e32 v86, 0
	s_waitcnt vmcnt(7)
	v_cvt_f16_f32_e32 v80, v102
	v_cvt_f16_f32_e32 v1, v103
	v_cvt_f16_f32_e32 v81, v108
	v_lshlrev_b32_e32 v87, 1, v0
	s_and_saveexec_b64 s[2:3], s[8:9]
	s_cbranch_execz .LBB4_14

.LBB4_16:
	s_or_b64 exec, exec, s[2:3]
	s_mov_b64 s[2:3], s[30:31]
	s_and_saveexec_b64 s[4:5], vcc
	s_cbranch_execnz .LBB4_19
	s_branch .LBB4_25

.LBB4_18:
	s_movk_i32 s4, 0x667
	v_mov_b32_e32 v1, 0xcce00
	v_mad_u32_u24 v1, v0, s4, v1
	s_movk_i32 s4, 0x90
	v_mul_u32_u24_sdwa v22, v1, s4 dst_sel:DWORD dst_unused:UNUSED_PAD src0_sel:WORD_1 src1_sel:DWORD
	s_movk_i32 s4, 0xffb0
	v_mul_i32_i24_sdwa v1, v1, s4 dst_sel:DWORD dst_unused:UNUSED_PAD src0_sel:WORD_1 src1_sel:DWORD
	v_lshlrev_b32_e32 v71, 1, v0
	v_add3_u32 v1, v22, v1, v71
	ds_write_b16 v1, v81 offset:9280
	s_or_b64 exec, exec, s[2:3]
	s_mov_b64 s[2:3], s[30:31]
	s_and_saveexec_b64 s[4:5], vcc
	s_cbranch_execz .LBB4_25

.LBB4_25:
	s_or_b64 exec, exec, s[4:5]
	v_and_b32_e32 v0, 15, v0
	s_movk_i32 s0, 0x90
	v_mad_u32_u24 v1, v0, s0, v72
	s_waitcnt lgkmcnt(0)
	s_barrier
	ds_read_b128 v[94:97], v1 offset:8256
	ds_read_b128 v[98:101], v1 offset:8320
	s_waitcnt vmcnt(4) lgkmcnt(1)
	v_mfma_f32_16x16x32_f16 a[0:3], v[94:97], v[6:9], 0
	v_lshlrev_b32_e32 v0, 2, v0
	s_movk_i32 s0, 0x810
	v_lshl_or_b32 v0, s16, 7, v0
	s_waitcnt vmcnt(3)
	v_mfma_f32_16x16x32_f16 a[4:7], v[94:97], v[38:41], 0
	v_mad_u32_u24 v0, v82, s0, v0
	s_movk_i32 s0, 0x204
	s_waitcnt lgkmcnt(0)
	v_mfma_f32_16x16x32_f16 a[0:3], v[98:101], v[90:93], a[0:3]
	v_mad_u32_u24 v38, v84, s0, v85
	s_waitcnt vmcnt(2)
	v_cvt_f32_f16_sdwa v1, v46 dst_sel:DWORD dst_unused:UNUSED_PAD src0_sel:WORD_1
	v_cvt_f32_f16_sdwa v9, v47 dst_sel:DWORD dst_unused:UNUSED_PAD src0_sel:WORD_1
	v_mfma_f32_16x16x32_f16 a[4:7], v[98:101], v[104:107], a[4:7]
	s_nop 2
	ds_write_b32 v0, a0
	ds_write_b32 v0, a1 offset:516
	ds_write_b32 v0, a2 offset:1032
	ds_write_b32 v0, a3 offset:1548
	s_nop 0
	ds_write_b32 v0, a4 offset:64
	ds_write_b32 v0, a5 offset:580
	ds_write_b32 v0, a6 offset:1096
	ds_write_b32 v0, a7 offset:1612
	s_waitcnt lgkmcnt(0)
	s_barrier
	ds_read2_b32 v[6:7], v38 offset1:1
	v_cvt_f32_f16_e32 v0, v46
	v_cvt_f32_f16_e32 v8, v47
	ds_read2_b32 v[22:23], v38 offset0:2 offset1:3
	ds_read2_b32 v[24:25], v38 offset0:4 offset1:5
	ds_read2_b32 v[38:39], v38 offset0:6 offset1:7
	v_mov_b32_e32 v71, 0
	s_waitcnt vmcnt(0) lgkmcnt(3)
	v_pk_fma_f32 v[0:1], v[50:51], v[6:7], v[0:1]
	s_andn2_b64 vcc, exec, s[6:7]
	v_cvt_pk_f16_f32 v6, v0, v1
	s_waitcnt lgkmcnt(2)
	v_pk_fma_f32 v[0:1], v[52:53], v[22:23], v[8:9]
	v_cvt_f32_f16_sdwa v9, v48 dst_sel:DWORD dst_unused:UNUSED_PAD src0_sel:WORD_1
	v_cvt_f32_f16_e32 v8, v48
	v_cvt_f32_f16_sdwa v23, v49 dst_sel:DWORD dst_unused:UNUSED_PAD src0_sel:WORD_1
	v_cvt_f32_f16_e32 v22, v49
	v_cvt_pk_f16_f32 v7, v0, v1
	s_waitcnt lgkmcnt(1)
	v_pk_fma_f32 v[0:1], v[42:43], v[24:25], v[8:9]
	s_nop 0
	v_cvt_pk_f16_f32 v8, v0, v1
	s_waitcnt lgkmcnt(0)
	v_pk_fma_f32 v[0:1], v[44:45], v[38:39], v[22:23]
	s_nop 0
	v_cvt_pk_f16_f32 v9, v0, v1
	v_lshl_add_u64 v[0:1], v[78:79], 1, s[2:3]
	v_lshl_add_u64 v[0:1], v[0:1], 0, v[70:71]
	global_store_dwordx4 v[0:1], v[6:9], off
	s_cbranch_vccnz .LBB4_27
	s_nop 0
	v_add_f32_e32 v6, v73, v75
	v_add_f32_e32 v6, v6, v83
	v_add_f32_e32 v22, v6, v86
	v_div_scale_f32 v23, s[0:1], v22, v22, 1.0
	v_rcp_f32_e32 v24, v23
	v_pk_add_f32 v[6:7], v[12:13], v[60:61]
	v_pk_add_f32 v[0:1], v[10:11], v[58:59]
	v_pk_add_f32 v[8:9], v[34:35], v[54:55]
	v_fma_f32 v12, -v23, v24, 1.0
	v_fmac_f32_e32 v24, v12, v24
	v_div_scale_f32 v12, vcc, 1.0, v22, 1.0
	v_mul_f32_e32 v13, v12, v24
	v_fma_f32 v25, -v23, v13, v12
	v_fmac_f32_e32 v13, v25, v24
	v_fma_f32 v12, -v23, v13, v12
	v_div_fmas_f32 v12, v12, v24, v13
	v_div_fixup_f32 v12, v12, v22, 1.0
	v_cvt_f32_f16_sdwa v23, v2 dst_sel:DWORD dst_unused:UNUSED_PAD src0_sel:WORD_1
	v_cvt_f32_f16_e32 v22, v2
	v_pk_add_f32 v[0:1], v[0:1], v[14:15]
	v_cvt_f32_f16_sdwa v15, v3 dst_sel:DWORD dst_unused:UNUSED_PAD src0_sel:WORD_1
	v_cvt_f32_f16_e32 v14, v3
	v_pk_add_f32 v[2:3], v[6:7], v[16:17]
	v_pk_add_f32 v[0:1], v[0:1], v[62:63]
	v_pk_add_f32 v[2:3], v[2:3], v[64:65]
	v_pk_mul_f32 v[0:1], v[26:27], v[0:1]
	v_pk_mul_f32 v[2:3], v[28:29], v[2:3]
	v_pk_fma_f32 v[0:1], v[0:1], v[12:13], v[22:23] op_sel_hi:[1,0,1]
	v_pk_fma_f32 v[2:3], v[2:3], v[12:13], v[14:15] op_sel_hi:[1,0,1]
	v_cvt_pk_f16_f32 v0, v0, v1
	v_cvt_pk_f16_f32 v1, v2, v3
	v_cvt_f32_f16_sdwa v3, v4 dst_sel:DWORD dst_unused:UNUSED_PAD src0_sel:WORD_1
	v_cvt_f32_f16_e32 v2, v4
	v_pk_add_f32 v[6:7], v[8:9], v[18:19]
	v_pk_add_f32 v[10:11], v[36:37], v[56:57]
	v_pk_add_f32 v[6:7], v[6:7], v[66:67]
	s_movk_i32 s0, 0x140
	v_pk_mul_f32 v[6:7], v[30:31], v[6:7]
	v_mov_b32_e32 v75, v71
	v_pk_fma_f32 v[2:3], v[6:7], v[12:13], v[2:3] op_sel_hi:[1,0,1]
	v_cvt_f32_f16_sdwa v7, v5 dst_sel:DWORD dst_unused:UNUSED_PAD src0_sel:WORD_1
	v_cvt_f32_f16_e32 v6, v5
	v_pk_add_f32 v[4:5], v[10:11], v[20:21]
	v_cvt_pk_f16_f32 v2, v2, v3
	v_pk_add_f32 v[4:5], v[4:5], v[68:69]
	s_nop 0
	v_pk_mul_f32 v[4:5], v[32:33], v[4:5]
	s_nop 0
	v_pk_fma_f32 v[4:5], v[4:5], v[12:13], v[6:7] op_sel_hi:[1,0,1]
	s_nop 0
	v_cvt_pk_f16_f32 v3, v4, v5
	v_mov_b64_e32 v[4:5], s[2:3]
	v_mad_u64_u32 v[4:5], s[0:1], v76, s0, v[4:5]
	v_lshl_add_u64 v[4:5], v[4:5], 0, v[74:75]
	global_store_dwordx4 v[4:5], v[0:3], off offset:256

	.amdhsa_kernel _Z8k_resid2PKDF16_PKfS0_S2_S2_PDF16_
		.amdhsa_group_segment_fixed_size 10560
		.amdhsa_private_segment_fixed_size 0
		.amdhsa_kernarg_size 48
		.amdhsa_user_sgpr_count 2
		.amdhsa_user_sgpr_dispatch_ptr 0
		.amdhsa_user_sgpr_queue_ptr 0
		.amdhsa_user_sgpr_kernarg_segment_ptr 1
		.amdhsa_user_sgpr_dispatch_id 0
		.amdhsa_user_sgpr_kernarg_preload_length 0
		.amdhsa_user_sgpr_kernarg_preload_offset 0
		.amdhsa_user_sgpr_private_segment_size 0
		.amdhsa_uses_dynamic_stack 0
		.amdhsa_enable_private_segment 0
		.amdhsa_system_sgpr_workgroup_id_x 1
		.amdhsa_system_sgpr_workgroup_id_y 0
		.amdhsa_system_sgpr_workgroup_id_z 0
		.amdhsa_system_sgpr_workgroup_info 0
		.amdhsa_system_vgpr_workitem_id 0
		.amdhsa_next_free_vgpr 120
		.amdhsa_next_free_sgpr 32
		.amdhsa_accum_offset 112
		.amdhsa_reserve_vcc 1
		.amdhsa_float_round_mode_32 0
		.amdhsa_float_round_mode_16_64 0
		.amdhsa_float_denorm_mode_32 3
		.amdhsa_float_denorm_mode_16_64 3
		.amdhsa_dx10_clamp 1
		.amdhsa_ieee_mode 1
		.amdhsa_fp16_overflow 0
		.amdhsa_tg_split 0
		.amdhsa_exception_fp_ieee_invalid_op 0
		.amdhsa_exception_fp_denorm_src 0
		.amdhsa_exception_fp_ieee_div_zero 0
		.amdhsa_exception_fp_ieee_overflow 0
		.amdhsa_exception_fp_ieee_underflow 0
		.amdhsa_exception_fp_ieee_inexact 0
		.amdhsa_exception_int_div_zero 0
	.end_amdhsa_kernel

amdhsa.kernels:
  - .agpr_count:     0
    .args:
      - .actual_access:  read_only
        .address_space:  global
        .offset:         0
        .size:           8
        .value_kind:     global_buffer
      - .actual_access:  read_only
        .address_space:  global
        .offset:         8
        .size:           8
        .value_kind:     global_buffer
      - .actual_access:  read_only
        .address_space:  global
        .offset:         16
        .size:           8
        .value_kind:     global_buffer
      - .actual_access:  read_only
        .address_space:  global
        .offset:         24
        .size:           8
        .value_kind:     global_buffer
      - .actual_access:  read_only
        .address_space:  global
        .offset:         32
        .size:           8
        .value_kind:     global_buffer
      - .actual_access:  read_only
        .address_space:  global
        .offset:         40
        .size:           8
        .value_kind:     global_buffer
      - .actual_access:  read_only
        .address_space:  global
        .offset:         48
        .size:           8
        .value_kind:     global_buffer
      - .actual_access:  write_only
        .address_space:  global
        .offset:         56
        .size:           8
        .value_kind:     global_buffer
    .group_segment_fixed_size: 98304
    .kernarg_segment_align: 8
    .kernarg_segment_size: 64
    .language:       OpenCL C
    .language_version:
      - 2
      - 0
    .max_flat_workgroup_size: 512
    .name:           _Z11k_conv_mfmaPKDF16_PKDv8_DF16_PKfS5_S5_S5_S5_PDF16_
    .private_segment_fixed_size: 0
    .sgpr_count:     36
    .sgpr_spill_count: 0
    .symbol:         _Z11k_conv_mfmaPKDF16_PKDv8_DF16_PKfS5_S5_S5_S5_PDF16_.kd
    .uniform_work_group_size: 1
    .uses_dynamic_stack: false
    .vgpr_count:     164
    .vgpr_spill_count: 0
    .wavefront_size: 64
  - .agpr_count:     0
    .args:
      - .actual_access:  read_only
        .address_space:  global
        .offset:         0
        .size:           8
        .value_kind:     global_buffer
      - .actual_access:  read_only
        .address_space:  global
        .offset:         8
        .size:           8
        .value_kind:     global_buffer
      - .actual_access:  read_only
        .address_space:  global
        .offset:         16
        .size:           8
        .value_kind:     global_buffer
      - .actual_access:  write_only
        .address_space:  global
        .offset:         24
        .size:           8
        .value_kind:     global_buffer
    .group_segment_fixed_size: 25600
    .kernarg_segment_align: 8
    .kernarg_segment_size: 32
    .language:       OpenCL C
    .language_version:
      - 2
      - 0
    .max_flat_workgroup_size: 1024
    .name:           _Z12k_recon_mfmaPKDF16_PKDv8_DF16_PKfPf
    .private_segment_fixed_size: 0
    .sgpr_count:     25
    .sgpr_spill_count: 0
    .symbol:         _Z12k_recon_mfmaPKDF16_PKDv8_DF16_PKfPf.kd
    .uniform_work_group_size: 1
    .uses_dynamic_stack: false
    .vgpr_count:     84
    .vgpr_spill_count: 0
    .wavefront_size: 64
  - .agpr_count:     0
    .args:
      - .actual_access:  read_only
        .address_space:  global
        .offset:         0
        .size:           8
        .value_kind:     global_buffer
      - .actual_access:  read_only
        .address_space:  global
        .offset:         8
        .size:           8
        .value_kind:     global_buffer
      - .actual_access:  read_only
        .address_space:  global
        .offset:         16
        .size:           8
        .value_kind:     global_buffer
      - .actual_access:  write_only
        .address_space:  global
        .offset:         24
        .size:           8
        .value_kind:     global_buffer
      - .actual_access:  write_only
        .address_space:  global
        .offset:         32
        .size:           8
        .value_kind:     global_buffer
      - .actual_access:  write_only
        .address_space:  global
        .offset:         40
        .size:           8
        .value_kind:     global_buffer
      - .actual_access:  write_only
        .address_space:  global
        .offset:         48
        .size:           8
        .value_kind:     global_buffer
      - .actual_access:  write_only
        .address_space:  global
        .offset:         56
        .size:           8
        .value_kind:     global_buffer
      - .actual_access:  write_only
        .address_space:  global
        .offset:         64
        .size:           8
        .value_kind:     global_buffer
    .group_segment_fixed_size: 67600
    .kernarg_segment_align: 8
    .kernarg_segment_size: 72
    .language:       OpenCL C
    .language_version:
      - 2
      - 0
    .max_flat_workgroup_size: 512
    .name:           _Z11k_proj_mfmaPKDF16_PKDv8_DF16_PKfPfPS1_S6_PhS6_PDF16_
    .private_segment_fixed_size: 0
    .sgpr_count:     36
    .sgpr_spill_count: 0
    .symbol:         _Z11k_proj_mfmaPKDF16_PKDv8_DF16_PKfPfPS1_S6_PhS6_PDF16_.kd
    .uniform_work_group_size: 1
    .uses_dynamic_stack: false
    .vgpr_count:     155
    .vgpr_spill_count: 0
    .wavefront_size: 64
  - .agpr_count:     0
    .args:
      - .actual_access:  read_only
        .address_space:  global
        .offset:         0
        .size:           8
        .value_kind:     global_buffer
      - .actual_access:  read_only
        .address_space:  global
        .offset:         8
        .size:           8
        .value_kind:     global_buffer
      - .actual_access:  read_only
        .address_space:  global
        .offset:         16
        .size:           8
        .value_kind:     global_buffer
      - .actual_access:  read_only
        .address_space:  global
        .offset:         24
        .size:           8
        .value_kind:     global_buffer
      - .actual_access:  read_only
        .address_space:  global
        .offset:         32
        .size:           8
        .value_kind:     global_buffer
      - .actual_access:  read_only
        .address_space:  global
        .offset:         40
        .size:           8
        .value_kind:     global_buffer
      - .actual_access:  write_only
        .address_space:  global
        .offset:         48
        .size:           8
        .value_kind:     global_buffer
      - .actual_access:  write_only
        .address_space:  global
        .offset:         56
        .size:           8
        .value_kind:     global_buffer
      - .actual_access:  read_only
        .address_space:  global
        .offset:         64
        .size:           8
        .value_kind:     global_buffer
      - .actual_access:  read_only
        .address_space:  global
        .offset:         72
        .size:           8
        .value_kind:     global_buffer
      - .actual_access:  write_only
        .address_space:  global
        .offset:         80
        .size:           8
        .value_kind:     global_buffer
      - .actual_access:  write_only
        .address_space:  global
        .offset:         88
        .size:           8
        .value_kind:     global_buffer
    .group_segment_fixed_size: 65536
    .kernarg_segment_align: 8
    .kernarg_segment_size: 96
    .language:       OpenCL C
    .language_version:
      - 2
      - 0
    .max_flat_workgroup_size: 512
    .name:           _Z6k_attnPKDv8_DF16_PKfPKhS3_S3_S3_PfS6_S3_S3_PS_S7_
    .private_segment_fixed_size: 0
    .sgpr_count:     34
    .sgpr_spill_count: 0
    .symbol:         _Z6k_attnPKDv8_DF16_PKfPKhS3_S3_S3_PfS6_S3_S3_PS_S7_.kd
    .uniform_work_group_size: 1
    .uses_dynamic_stack: false
    .vgpr_count:     126
    .vgpr_spill_count: 0
    .wavefront_size: 64
  - .agpr_count:     8
    .args:
      - .actual_access:  read_only
        .address_space:  global
        .offset:         0
        .size:           8
        .value_kind:     global_buffer
      - .actual_access:  read_only
        .address_space:  global
        .offset:         8
        .size:           8
        .value_kind:     global_buffer
      - .actual_access:  read_only
        .address_space:  global
        .offset:         16
        .size:           8
        .value_kind:     global_buffer
      - .actual_access:  read_only
        .address_space:  global
        .offset:         24
        .size:           8
        .value_kind:     global_buffer
      - .actual_access:  read_only
        .address_space:  global
        .offset:         32
        .size:           8
        .value_kind:     global_buffer
      - .actual_access:  write_only
        .address_space:  global
        .offset:         40
        .size:           8
        .value_kind:     global_buffer
    .group_segment_fixed_size: 10560
    .kernarg_segment_align: 8
    .kernarg_segment_size: 48
    .language:       OpenCL C
    .language_version:
      - 2
      - 0
    .max_flat_workgroup_size: 256
    .name:           _Z8k_resid2PKDF16_PKfS0_S2_S2_PDF16_
    .private_segment_fixed_size: 0
    .sgpr_count:     38
    .sgpr_spill_count: 0
    .symbol:         _Z8k_resid2PKDF16_PKfS0_S2_S2_PDF16_.kd
    .uniform_work_group_size: 1
    .uses_dynamic_stack: false
    .vgpr_count:     120
    .vgpr_spill_count: 0
    .wavefront_size: 64
  - .agpr_count:     0
    .args:
      - .actual_access:  read_only
        .address_space:  global
        .offset:         0
        .size:           8
        .value_kind:     global_buffer
      - .actual_access:  read_only
        .address_space:  global
        .offset:         8
        .size:           8
        .value_kind:     global_buffer
      - .actual_access:  read_only
        .address_space:  global
        .offset:         16
        .size:           8
        .value_kind:     global_buffer
      - .actual_access:  read_only
        .address_space:  global
        .offset:         24
        .size:           8
        .value_kind:     global_buffer
      - .actual_access:  read_only
        .address_space:  global
        .offset:         32
        .size:           8
        .value_kind:     global_buffer
      - .actual_access:  read_only
        .address_space:  global
        .offset:         40
        .size:           8
        .value_kind:     global_buffer
      - .actual_access:  read_only
        .address_space:  global
        .offset:         48
        .size:           8
        .value_kind:     global_buffer
      - .actual_access:  read_only
        .address_space:  global
        .offset:         56
        .size:           8
        .value_kind:     global_buffer
      - .actual_access:  read_only
        .address_space:  global
        .offset:         64
        .size:           8
        .value_kind:     global_buffer
      - .actual_access:  read_only
        .address_space:  global
        .offset:         72
        .size:           8
        .value_kind:     global_buffer
      - .actual_access:  write_only
        .address_space:  global
        .offset:         80
        .size:           8
        .value_kind:     global_buffer
      - .actual_access:  read_only
        .address_space:  global
        .offset:         88
        .size:           8
        .value_kind:     global_buffer
      - .actual_access:  read_only
        .address_space:  global
        .offset:         96
        .size:           8
        .value_kind:     global_buffer
      - .actual_access:  read_only
        .address_space:  global
        .offset:         104
        .size:           8
        .value_kind:     global_buffer
      - .actual_access:  read_only
        .address_space:  global
        .offset:         112
        .size:           8
        .value_kind:     global_buffer
      - .actual_access:  read_only
        .address_space:  global
        .offset:         120
        .size:           8
        .value_kind:     global_buffer
      - .actual_access:  read_only
        .address_space:  global
        .offset:         128
        .size:           8
        .value_kind:     global_buffer
      - .actual_access:  write_only
        .address_space:  global
        .offset:         136
        .size:           8
        .value_kind:     global_buffer
    .group_segment_fixed_size: 21248
    .kernarg_segment_align: 8
    .kernarg_segment_size: 144
    .language:       OpenCL C
    .language_version:
      - 2
      - 0
    .max_flat_workgroup_size: 512
    .name:           _Z8k_embed2PKfS0_S0_S0_S0_S0_S0_S0_S0_S0_PDF16_S0_S0_S0_S0_S0_S0_PDv8_DF16_
    .private_segment_fixed_size: 0
    .sgpr_count:     37
    .sgpr_spill_count: 0
    .symbol:         _Z8k_embed2PKfS0_S0_S0_S0_S0_S0_S0_S0_S0_PDF16_S0_S0_S0_S0_S0_S0_PDv8_DF16_.kd
    .uniform_work_group_size: 1
    .uses_dynamic_stack: false
    .vgpr_count:     99
    .vgpr_spill_count: 0
    .wavefront_size: 64
